# speedup vs baseline: 1.0234x; 1.0063x over previous
.LBB1_13:
	s_or_b64 exec, exec, s[2:3]
	v_div_scale_f32 v66, s[0:1], v101, v101, 1.0
	v_rcp_f32_e32 v67, v66
	v_div_scale_f32 v68, vcc, 1.0, v101, 1.0
	v_fma_f32 v70, -v66, v67, 1.0
	v_fmac_f32_e32 v67, v70, v67
	v_mul_f32_e32 v70, v68, v67
	v_fma_f32 v71, -v66, v70, v68
	v_fmac_f32_e32 v70, v71, v67
	v_fma_f32 v66, -v66, v70, v68
	v_div_fmas_f32 v66, v66, v67, v70
	v_div_fixup_f32 v68, v66, v101, 1.0
	s_barrier
	v_lshrrev_b32_e32 v70, 4, v161
	v_and_b32_e32 v71, 15, v161
	v_lshrrev_b32_e32 v72, 3, v164
	v_and_b32_e32 v73, 15, v160
	v_xor_b32_e32 v72, v72, v73
	v_lshlrev_b32_e32 v72, 4, v72
	v_add_u32_e32 v73, v162, v160
	v_lshlrev_b32_e32 v73, 8, v73
	v_xor_b32_e32 v74, v71, v70
	v_lshlrev_b32_e32 v74, 4, v74
	v_add_u32_e32 v75, v162, v70
	v_lshlrev_b32_e32 v75, 8, v75
	v_or_b32_e32 v64, v64, v70
	v_lshlrev_b64 v[76:77], 8, v[64:65]
	v_lshl_add_u64 v[76:77], v[76:77], 0, s[24:25]
	v_lshlrev_b32_e32 v78, 4, v71
	v_mov_b32_e32 v79, 0
	v_lshl_add_u64 v[76:77], v[76:77], 0, v[78:79]
	s_mov_b64 s[2:3], 0x1000
	v_lshl_add_u64 v[78:79], v[76:77], 0, s[2:3]
	v_mul_f32_e32 v48, v68, v48
	v_mul_f32_e32 v49, v68, v49
	v_mul_f32_e32 v50, v68, v50
	v_mul_f32_e32 v51, v68, v51
	v_mul_f32_e32 v52, v68, v52
	v_mul_f32_e32 v53, v68, v53
	v_mul_f32_e32 v54, v68, v54
	v_mul_f32_e32 v55, v68, v55
	v_cvt_pk_f16_f32 v48, v48, v49
	v_cvt_pk_f16_f32 v49, v50, v51
	v_cvt_pk_f16_f32 v50, v52, v53
	v_cvt_pk_f16_f32 v51, v54, v55
	v_xor_b32_e32 v80, 0x0, v72
	v_add_u32_e32 v80, v80, v73
	v_permlane32_swap_b32_e32 v48, v50
	v_permlane32_swap_b32_e32 v49, v51
	ds_write_b128 v80, v[48:51]
	v_mul_f32_e32 v56, v68, v56
	v_mul_f32_e32 v57, v68, v57
	v_mul_f32_e32 v58, v68, v58
	v_mul_f32_e32 v59, v68, v59
	v_mul_f32_e32 v60, v68, v60
	v_mul_f32_e32 v61, v68, v61
	v_mul_f32_e32 v62, v68, v62
	v_mul_f32_e32 v63, v68, v63
	v_cvt_pk_f16_f32 v56, v56, v57
	v_cvt_pk_f16_f32 v57, v58, v59
	v_cvt_pk_f16_f32 v58, v60, v61
	v_cvt_pk_f16_f32 v59, v62, v63
	v_xor_b32_e32 v80, 0x20, v72
	v_add_u32_e32 v80, v80, v73
	v_permlane32_swap_b32_e32 v56, v58
	v_permlane32_swap_b32_e32 v57, v59
	ds_write_b128 v80, v[56:59]
	v_mul_f32_e32 v32, v68, v32
	v_mul_f32_e32 v33, v68, v33
	v_mul_f32_e32 v34, v68, v34
	v_mul_f32_e32 v35, v68, v35
	v_mul_f32_e32 v36, v68, v36
	v_mul_f32_e32 v37, v68, v37
	v_mul_f32_e32 v38, v68, v38
	v_mul_f32_e32 v39, v68, v39
	v_cvt_pk_f16_f32 v32, v32, v33
	v_cvt_pk_f16_f32 v33, v34, v35
	v_cvt_pk_f16_f32 v34, v36, v37
	v_cvt_pk_f16_f32 v35, v38, v39
	v_xor_b32_e32 v80, 0x40, v72
	v_add_u32_e32 v80, v80, v73
	v_permlane32_swap_b32_e32 v32, v34
	v_permlane32_swap_b32_e32 v33, v35
	ds_write_b128 v80, v[32:35]
	v_mul_f32_e32 v40, v68, v40
	v_mul_f32_e32 v41, v68, v41
	v_mul_f32_e32 v42, v68, v42
	v_mul_f32_e32 v43, v68, v43
	v_mul_f32_e32 v44, v68, v44
	v_mul_f32_e32 v45, v68, v45
	v_mul_f32_e32 v46, v68, v46
	v_mul_f32_e32 v47, v68, v47
	v_cvt_pk_f16_f32 v40, v40, v41
	v_cvt_pk_f16_f32 v41, v42, v43
	v_cvt_pk_f16_f32 v42, v44, v45
	v_cvt_pk_f16_f32 v43, v46, v47
	v_xor_b32_e32 v80, 0x60, v72
	v_add_u32_e32 v80, v80, v73
	v_permlane32_swap_b32_e32 v40, v42
	v_permlane32_swap_b32_e32 v41, v43
	ds_write_b128 v80, v[40:43]
	v_mul_f32_e32 v16, v68, v16
	v_mul_f32_e32 v17, v68, v17
	v_mul_f32_e32 v18, v68, v18
	v_mul_f32_e32 v19, v68, v19
	v_mul_f32_e32 v20, v68, v20
	v_mul_f32_e32 v21, v68, v21
	v_mul_f32_e32 v22, v68, v22
	v_mul_f32_e32 v23, v68, v23
	v_cvt_pk_f16_f32 v16, v16, v17
	v_cvt_pk_f16_f32 v17, v18, v19
	v_cvt_pk_f16_f32 v18, v20, v21
	v_cvt_pk_f16_f32 v19, v22, v23
	v_xor_b32_e32 v80, 0x80, v72
	v_add_u32_e32 v80, v80, v73
	v_permlane32_swap_b32_e32 v16, v18
	v_permlane32_swap_b32_e32 v17, v19
	ds_write_b128 v80, v[16:19]
	v_mul_f32_e32 v24, v68, v24
	v_mul_f32_e32 v25, v68, v25
	v_mul_f32_e32 v26, v68, v26
	v_mul_f32_e32 v27, v68, v27
	v_mul_f32_e32 v28, v68, v28
	v_mul_f32_e32 v29, v68, v29
	v_mul_f32_e32 v30, v68, v30
	v_mul_f32_e32 v31, v68, v31
	v_cvt_pk_f16_f32 v24, v24, v25
	v_cvt_pk_f16_f32 v25, v26, v27
	v_cvt_pk_f16_f32 v26, v28, v29
	v_cvt_pk_f16_f32 v27, v30, v31
	v_xor_b32_e32 v80, 0xa0, v72
	v_add_u32_e32 v80, v80, v73
	v_permlane32_swap_b32_e32 v24, v26
	v_permlane32_swap_b32_e32 v25, v27
	ds_write_b128 v80, v[24:27]
	v_mul_f32_e32 v0, v68, v0
	v_mul_f32_e32 v1, v68, v1
	v_mul_f32_e32 v2, v68, v2
	v_mul_f32_e32 v3, v68, v3
	v_mul_f32_e32 v4, v68, v4
	v_mul_f32_e32 v5, v68, v5
	v_mul_f32_e32 v6, v68, v6
	v_mul_f32_e32 v7, v68, v7
	v_cvt_pk_f16_f32 v0, v0, v1
	v_cvt_pk_f16_f32 v1, v2, v3
	v_cvt_pk_f16_f32 v2, v4, v5
	v_cvt_pk_f16_f32 v3, v6, v7
	v_xor_b32_e32 v80, 0xc0, v72
	v_add_u32_e32 v80, v80, v73
	v_permlane32_swap_b32_e32 v0, v2
	v_permlane32_swap_b32_e32 v1, v3
	ds_write_b128 v80, v[0:3]
	v_mul_f32_e32 v8, v68, v8
	v_mul_f32_e32 v9, v68, v9
	v_mul_f32_e32 v10, v68, v10
	v_mul_f32_e32 v11, v68, v11
	v_mul_f32_e32 v12, v68, v12
	v_mul_f32_e32 v13, v68, v13
	v_mul_f32_e32 v14, v68, v14
	v_mul_f32_e32 v15, v68, v15
	v_cvt_pk_f16_f32 v8, v8, v9
	v_cvt_pk_f16_f32 v9, v10, v11
	v_cvt_pk_f16_f32 v10, v12, v13
	v_cvt_pk_f16_f32 v11, v14, v15
	v_xor_b32_e32 v80, 0xe0, v72
	v_add_u32_e32 v80, v80, v73
	v_permlane32_swap_b32_e32 v8, v10
	v_permlane32_swap_b32_e32 v9, v11
	ds_write_b128 v80, v[8:11]
	s_waitcnt lgkmcnt(0)
	v_xor_b32_e32 v81, 0x0, v74
	v_add_u32_e32 v81, v81, v75
	ds_read_b128 v[88:91], v81 offset:0
	v_xor_b32_e32 v81, 0x40, v74
	v_add_u32_e32 v81, v81, v75
	ds_read_b128 v[92:95], v81 offset:1024
	v_xor_b32_e32 v81, 0x80, v74
	v_add_u32_e32 v81, v81, v75
	ds_read_b128 v[96:99], v81 offset:2048
	v_xor_b32_e32 v81, 0xc0, v74
	v_add_u32_e32 v81, v81, v75
	ds_read_b128 v[100:103], v81 offset:3072
	v_xor_b32_e32 v81, 0x0, v74
	v_add_u32_e32 v81, v81, v75
	ds_read_b128 v[104:107], v81 offset:4096
	v_xor_b32_e32 v81, 0x40, v74
	v_add_u32_e32 v81, v81, v75
	ds_read_b128 v[108:111], v81 offset:5120
	v_xor_b32_e32 v81, 0x80, v74
	v_add_u32_e32 v81, v81, v75
	ds_read_b128 v[112:115], v81 offset:6144
	v_xor_b32_e32 v81, 0xc0, v74
	v_add_u32_e32 v81, v81, v75
	ds_read_b128 v[116:119], v81 offset:7168
	s_waitcnt lgkmcnt(7)
	global_store_dwordx4 v[76:77], v[88:91], off offset:0 sc1
	s_waitcnt lgkmcnt(6)
	global_store_dwordx4 v[76:77], v[92:95], off offset:1024 sc1
	s_waitcnt lgkmcnt(5)
	global_store_dwordx4 v[76:77], v[96:99], off offset:2048 sc1
	s_waitcnt lgkmcnt(4)
	global_store_dwordx4 v[76:77], v[100:103], off offset:3072 sc1
	s_waitcnt lgkmcnt(3)
	global_store_dwordx4 v[78:79], v[104:107], off offset:0 sc1
	s_waitcnt lgkmcnt(2)
	global_store_dwordx4 v[78:79], v[108:111], off offset:1024 sc1
	s_waitcnt lgkmcnt(1)
	global_store_dwordx4 v[78:79], v[112:115], off offset:2048 sc1
	s_waitcnt lgkmcnt(0)
	global_store_dwordx4 v[78:79], v[116:119], off offset:3072 sc1
	s_endpgm

	.amdhsa_kernel _Z11attn_kernelPKDF16_S0_PDF16_P15HIP_vector_typeIfLj2EE
		.amdhsa_group_segment_fixed_size 16384
		.amdhsa_private_segment_fixed_size 0
		.amdhsa_kernarg_size 32
		.amdhsa_user_sgpr_count 2
		.amdhsa_user_sgpr_dispatch_ptr 0
		.amdhsa_user_sgpr_queue_ptr 0
		.amdhsa_user_sgpr_kernarg_segment_ptr 1
		.amdhsa_user_sgpr_dispatch_id 0
		.amdhsa_user_sgpr_kernarg_preload_length 0
		.amdhsa_user_sgpr_kernarg_preload_offset 0
		.amdhsa_user_sgpr_private_segment_size 0
		.amdhsa_uses_dynamic_stack 0
		.amdhsa_enable_private_segment 0
		.amdhsa_system_sgpr_workgroup_id_x 1
		.amdhsa_system_sgpr_workgroup_id_y 1
		.amdhsa_system_sgpr_workgroup_id_z 1
		.amdhsa_system_sgpr_workgroup_info 0
		.amdhsa_system_vgpr_workitem_id 0
		.amdhsa_next_free_vgpr 244
		.amdhsa_next_free_sgpr 40
		.amdhsa_accum_offset 244
		.amdhsa_reserve_vcc 1
		.amdhsa_float_round_mode_32 0
		.amdhsa_float_round_mode_16_64 0
		.amdhsa_float_denorm_mode_32 3
		.amdhsa_float_denorm_mode_16_64 3
		.amdhsa_dx10_clamp 1
		.amdhsa_ieee_mode 1
		.amdhsa_fp16_overflow 0
		.amdhsa_tg_split 0
		.amdhsa_exception_fp_ieee_invalid_op 0
		.amdhsa_exception_fp_denorm_src 0
		.amdhsa_exception_fp_ieee_div_zero 0
		.amdhsa_exception_fp_ieee_overflow 0
		.amdhsa_exception_fp_ieee_underflow 0
		.amdhsa_exception_fp_ieee_inexact 0
		.amdhsa_exception_int_div_zero 0
	.end_amdhsa_kernel

amdhsa.kernels:
  - .agpr_count:     32
    .args:
      - .actual_access:  read_only
        .address_space:  global
        .offset:         0
        .size:           8
        .value_kind:     global_buffer
      - .actual_access:  read_only
        .address_space:  global
        .offset:         8
        .size:           8
        .value_kind:     global_buffer
      - .actual_access:  read_only
        .address_space:  global
        .offset:         16
        .size:           8
        .value_kind:     global_buffer
      - .actual_access:  read_only
        .address_space:  global
        .offset:         24
        .size:           8
        .value_kind:     global_buffer
      - .actual_access:  write_only
        .address_space:  global
        .offset:         32
        .size:           8
        .value_kind:     global_buffer
      - .actual_access:  write_only
        .address_space:  global
        .offset:         40
        .size:           8
        .value_kind:     global_buffer
      - .actual_access:  read_only
        .address_space:  global
        .offset:         48
        .size:           8
        .value_kind:     global_buffer
      - .actual_access:  write_only
        .address_space:  global
        .offset:         56
        .size:           8
        .value_kind:     global_buffer
    .group_segment_fixed_size: 34816
    .kernarg_segment_align: 8
    .kernarg_segment_size: 64
    .language:       OpenCL C
    .language_version:
      - 2
      - 0
    .max_flat_workgroup_size: 256
    .name:           _Z11prep_kernelPKfS0_S0_S0_PDF16_S1_S0_S1_
    .private_segment_fixed_size: 0
    .sgpr_count:     30
    .sgpr_spill_count: 0
    .symbol:         _Z11prep_kernelPKfS0_S0_S0_PDF16_S1_S0_S1_.kd
    .uniform_work_group_size: 1
    .uses_dynamic_stack: false
    .vgpr_count:     220
    .vgpr_spill_count: 0
    .wavefront_size: 64
  - .agpr_count:     0
    .args:
      - .actual_access:  read_only
        .address_space:  global
        .offset:         0
        .size:           8
        .value_kind:     global_buffer
      - .address_space:  global
        .offset:         8
        .size:           8
        .value_kind:     global_buffer
      - .actual_access:  write_only
        .address_space:  global
        .offset:         16
        .size:           8
        .value_kind:     global_buffer
      - .actual_access:  write_only
        .address_space:  global
        .offset:         24
        .size:           8
        .value_kind:     global_buffer
    .group_segment_fixed_size: 16384
    .kernarg_segment_align: 8
    .kernarg_segment_size: 32
    .language:       OpenCL C
    .language_version:
      - 2
      - 0
    .max_flat_workgroup_size: 512
    .name:           _Z11attn_kernelPKDF16_S0_PDF16_P15HIP_vector_typeIfLj2EE
    .private_segment_fixed_size: 0
    .sgpr_count:     46
    .sgpr_spill_count: 0
    .symbol:         _Z11attn_kernelPKDF16_S0_PDF16_P15HIP_vector_typeIfLj2EE.kd
    .uniform_work_group_size: 1
    .uses_dynamic_stack: false
    .vgpr_count:     244
    .vgpr_spill_count: 0
    .wavefront_size: 64
  - .agpr_count:     0
    .args:
      - .actual_access:  read_only
        .address_space:  global
        .offset:         0
        .size:           8
        .value_kind:     global_buffer
      - .actual_access:  read_only
        .address_space:  global
        .offset:         8
        .size:           8
        .value_kind:     global_buffer
      - .actual_access:  read_only
        .address_space:  global
        .offset:         16
        .size:           8
        .value_kind:     global_buffer
      - .actual_access:  read_only
        .address_space:  global
        .offset:         24
        .size:           8
        .value_kind:     global_buffer
      - .actual_access:  write_only
        .address_space:  global
        .offset:         32
        .size:           8
        .value_kind:     global_buffer
    .group_segment_fixed_size: 17408
    .kernarg_segment_align: 8
    .kernarg_segment_size: 40
    .language:       OpenCL C
    .language_version:
      - 2
      - 0
    .max_flat_workgroup_size: 256
    .name:           _Z19combine_proj_kernelPKDF16_PK15HIP_vector_typeIfLj2EES0_PKfPf
    .private_segment_fixed_size: 0
    .sgpr_count:     42
    .sgpr_spill_count: 0
    .symbol:         _Z19combine_proj_kernelPKDF16_PK15HIP_vector_typeIfLj2EES0_PKfPf.kd
    .uniform_work_group_size: 1
    .uses_dynamic_stack: false
    .vgpr_count:     220
    .vgpr_spill_count: 0
    .wavefront_size: 64
